# rewritten k3 loop with sc1 (L2 no-keep) assign stores + L2 warm-up of codebook fragments
# speedup vs baseline: 1.0042x; 1.0042x over previous
.Lk3m_loop:
	s_waitcnt lgkmcnt(0)
	s_lshl_b32 s84, s70, 13
	s_add_u32 s90, s80, s84
	s_addc_u32 s91, s81, 0
	s_mul_i32 s84, s70, 0xc000
	s_add_u32 s92, s94, s84
	s_addc_u32 s93, s95, 0
	s_add_i32 s84, s70, 2
	s_and_b32 s84, s84, 15
	s_lshl_b32 s82, s84, 12
	s_lshl_b32 s84, s84, 16
	s_add_u32 s84, s84, 0x787000
	s_add_u32 s86, s40, s84
	s_addc_u32 s87, s41, 0
	s_add_u32 s88, s86, 0x1000
	s_addc_u32 s89, s87, 0
	s_add_i32 s84, s70, 15
	s_and_b32 s84, s84, 15
	s_mul_i32 s84, s84, 0xc0
	s_add_u32 s83, s84, 0x10000
	v_add_u32_e32 v112, s82, v105
	v_sub_f32_e32 v120, v94, v114
	v_cmp_eq_f32_e64 s[72:73], v94, v114
	s_waitcnt vmcnt(27)
	v_mfma_f32_16x16x4_f32 v[176:179], v132, v6, 0
	ds_read2st64_b32 v[254:255], v112 offset1:1
	v_sub_f32_e32 v121, v90, v114
	v_cmp_eq_f32_e64 s[74:75], v90, v114
	v_exp_f32_e32 v149, v120
	v_cndmask_b32_e64 v118, v155, 15, s[72:73]
	v_max3_f32 v115, v35, v39, v43
	v_sub_f32_e32 v120, v86, v114
	v_cmp_eq_f32_e64 s[76:77], v86, v114
	v_exp_f32_e32 v148, v121
	v_cndmask_b32_e64 v118, v118, 14, s[74:75]
	v_mfma_f32_16x16x4_f32 v[180:183], v132, v8, 0
	v_sub_f32_e32 v121, v82, v114
	v_max3_f32 v117, v47, v51, v55
	v_cmp_eq_f32_e64 s[72:73], v82, v114
	v_exp_f32_e32 v147, v120
	v_cndmask_b32_e64 v118, v118, 13, s[76:77]
	v_sub_f32_e32 v120, v78, v114
	v_cmp_eq_f32_e64 s[74:75], v78, v114
	v_max3_f32 v115, v115, v59, v63
	v_exp_f32_e32 v146, v121
	v_cndmask_b32_e64 v118, v118, 12, s[72:73]
	v_mfma_f32_16x16x4_f32 v[176:179], v133, v7, v[176:179]
	v_sub_f32_e32 v121, v74, v114
	v_cmp_eq_f32_e64 s[76:77], v74, v114
	v_exp_f32_e32 v145, v120
	v_cndmask_b32_e64 v118, v118, 11, s[74:75]
	v_max3_f32 v117, v117, v67, v71
	v_sub_f32_e32 v120, v70, v114
	v_cmp_eq_f32_e64 s[72:73], v70, v114
	v_exp_f32_e32 v144, v121
	v_cndmask_b32_e64 v118, v118, 10, s[76:77]
	v_mfma_f32_16x16x4_f32 v[180:183], v133, v9, v[180:183]
	global_load_dwordx4 v[6:9], v104, s[86:87]
	v_sub_f32_e32 v121, v66, v114
	v_max3_f32 v115, v115, v75, v79
	v_cmp_eq_f32_e64 s[74:75], v66, v114
	v_exp_f32_e32 v143, v120
	v_cndmask_b32_e64 v118, v118, 9, s[72:73]
	v_sub_f32_e32 v120, v62, v114
	v_cmp_eq_f32_e64 s[76:77], v62, v114
	v_max3_f32 v117, v117, v83, v87
	v_exp_f32_e32 v142, v121
	v_cndmask_b32_e64 v118, v118, 8, s[74:75]
	s_waitcnt vmcnt(27)
	v_mfma_f32_16x16x4_f32 v[184:187], v132, v2, 0
	v_sub_f32_e32 v121, v58, v114
	v_cmp_eq_f32_e64 s[72:73], v58, v114
	v_exp_f32_e32 v141, v120
	v_cndmask_b32_e64 v118, v118, 7, s[76:77]
	v_max3_f32 v115, v115, v91, v95
	v_sub_f32_e32 v120, v54, v114
	v_cmp_eq_f32_e64 s[74:75], v54, v114
	v_exp_f32_e32 v140, v121
	v_cndmask_b32_e64 v118, v118, 6, s[72:73]
	v_mfma_f32_16x16x4_f32 v[188:191], v132, v4, 0
	v_sub_f32_e32 v121, v50, v114
	v_max_f32_e32 v115, v115, v117
	v_cmp_eq_f32_e64 s[76:77], v50, v114
	v_exp_f32_e32 v139, v120
	v_cndmask_b32_e64 v118, v118, 5, s[74:75]
	v_sub_f32_e32 v120, v46, v114
	v_cmp_eq_f32_e64 s[72:73], v46, v114
	v_max_f32_dpp v115, v115, v115 row_ror:1 row_mask:0xf bank_mask:0xf
	v_exp_f32_e32 v138, v121
	v_cndmask_b32_e64 v118, v118, 4, s[76:77]
	v_mfma_f32_16x16x4_f32 v[184:187], v133, v3, v[184:187]
	v_sub_f32_e32 v121, v42, v114
	v_cmp_eq_f32_e64 s[74:75], v42, v114
	v_exp_f32_e32 v137, v120
	v_cndmask_b32_e64 v118, v118, 3, s[72:73]
	v_max_f32_dpp v115, v115, v115 row_ror:2 row_mask:0xf bank_mask:0xf
	v_sub_f32_e32 v120, v38, v114
	v_cmp_eq_f32_e64 s[76:77], v38, v114
	v_exp_f32_e32 v136, v121
	v_cndmask_b32_e64 v118, v118, 2, s[74:75]
	v_mfma_f32_16x16x4_f32 v[188:191], v133, v5, v[188:191]
	global_load_dwordx4 v[2:5], v104, s[86:87] offset:1024
	v_sub_f32_e32 v121, v34, v114
	v_max_f32_dpp v115, v115, v115 row_ror:4 row_mask:0xf bank_mask:0xf
	v_cmp_eq_f32_e64 s[72:73], v34, v114
	v_exp_f32_e32 v135, v120
	v_cndmask_b32_e64 v118, v118, 1, s[76:77]
	v_exp_f32_e32 v134, v121
	v_cndmask_b32_e64 v118, v118, 0, s[72:73]
	v_max_f32_dpp v115, v115, v115 row_ror:8 row_mask:0xf bank_mask:0xf
	v_sub_f32_e32 v120, v95, v115
	v_cmp_eq_f32_e64 s[72:73], v95, v115
	v_max3_f32 v114, v36, v40, v44
	s_waitcnt vmcnt(27)
	v_mfma_f32_16x16x4_f32 v[192:195], v132, v10, 0
	v_sub_f32_e32 v121, v91, v115
	v_and_b32_e32 v122, 12, v118
	v_cmp_eq_f32_e64 s[74:75], v91, v115
	v_and_b32_e32 v124, 3, v118
	v_exp_f32_e32 v175, v120
	v_add_f32_e32 v128, v134, v135
	v_cndmask_b32_e64 v119, v155, 15, s[72:73]
	v_add_f32_e32 v130, v136, v137
	v_sub_f32_e32 v120, v87, v115
	v_max3_f32 v116, v48, v52, v56
	v_cmp_eq_f32_e64 s[76:77], v87, v115
	v_exp_f32_e32 v174, v121
	v_lshl_or_b32 v122, v122, 4, v124
	v_cndmask_b32_e64 v119, v119, 14, s[74:75]
	v_add_f32_e32 v128, v128, v138
	v_mfma_f32_16x16x4_f32 v[196:199], v132, v12, 0
	v_sub_f32_e32 v121, v83, v115
	v_add_f32_e32 v130, v130, v139
	v_cmp_eq_f32_e64 s[72:73], v83, v115
	v_or_b32_e32 v122, v122, v102
	v_exp_f32_e32 v173, v120
	v_max3_f32 v114, v114, v60, v64
	v_cndmask_b32_e64 v119, v119, 13, s[76:77]
	v_add_f32_e32 v128, v128, v140
	v_sub_f32_e32 v120, v79, v115
	v_cmp_eq_f32_e64 s[74:75], v79, v115
	v_add_f32_e32 v130, v130, v141
	v_exp_f32_e32 v172, v121
	v_max_u32_e32 v126, v122, v118
	v_cndmask_b32_e64 v119, v119, 12, s[72:73]
	v_max3_f32 v116, v116, v68, v72
	v_mfma_f32_16x16x4_f32 v[192:195], v133, v11, v[192:195]
	v_sub_f32_e32 v121, v75, v115
	v_add_f32_e32 v128, v128, v142
	v_cmp_eq_f32_e64 s[76:77], v75, v115
	v_add_f32_e32 v130, v130, v143
	v_exp_f32_e32 v171, v120
	v_min_u32_dpp v126, v126, v126 row_ror:1 row_mask:0xf bank_mask:0xf
	v_cndmask_b32_e64 v119, v119, 11, s[74:75]
	v_sub_f32_e32 v120, v71, v115
	v_add_f32_e32 v128, v128, v144
	v_cmp_eq_f32_e64 s[72:73], v71, v115
	v_max3_f32 v114, v114, v76, v80
	v_exp_f32_e32 v170, v121
	v_add_f32_e32 v130, v130, v145
	v_cndmask_b32_e64 v119, v119, 10, s[76:77]
	v_min_u32_dpp v126, v126, v126 row_ror:2 row_mask:0xf bank_mask:0xf
	v_mfma_f32_16x16x4_f32 v[196:199], v133, v13, v[196:199]
	global_load_dwordx4 v[10:13], v104, s[86:87] offset:2048
	v_sub_f32_e32 v121, v67, v115
	v_add_f32_e32 v128, v128, v146
	v_cmp_eq_f32_e64 s[74:75], v67, v115
	v_max3_f32 v116, v116, v84, v88
	v_exp_f32_e32 v169, v120
	v_cndmask_b32_e64 v119, v119, 9, s[72:73]
	v_add_f32_e32 v130, v130, v147
	v_sub_f32_e32 v120, v63, v115
	v_min_u32_dpp v126, v126, v126 row_ror:4 row_mask:0xf bank_mask:0xf
	v_cmp_eq_f32_e64 s[76:77], v63, v115
	v_add_f32_e32 v128, v128, v148
	v_exp_f32_e32 v168, v121
	v_add_f32_e32 v130, v130, v149
	v_cndmask_b32_e64 v119, v119, 8, s[74:75]
	v_max3_f32 v114, v114, v92, v96
	s_waitcnt vmcnt(24)
	v_mfma_f32_16x16x4_f32 v[200:203], v132, v14, 0
	v_sub_f32_e32 v121, v59, v115
	v_min_u32_dpp v126, v126, v126 row_ror:8 row_mask:0xf bank_mask:0xf
	v_cmp_eq_f32_e64 s[72:73], v59, v115
	v_exp_f32_e32 v167, v120
	v_add_f32_e32 v128, v128, v130
	v_cndmask_b32_e64 v119, v119, 7, s[76:77]
	v_mad_u32_u24 v248, v126, 24, v107
	v_sub_f32_e32 v120, v55, v115
	v_add_f32_dpp v128, v128, v128 row_ror:1 row_mask:0xf bank_mask:0xf
	v_cmp_eq_f32_e64 s[74:75], v55, v115
	v_max_f32_e32 v114, v114, v116
	v_exp_f32_e32 v166, v121
	global_load_dword v240, v248, s[92:93]
	v_cndmask_b32_e64 v119, v119, 6, s[72:73]
	v_add_f32_dpp v128, v128, v128 row_ror:2 row_mask:0xf bank_mask:0xf
	v_mfma_f32_16x16x4_f32 v[204:207], v132, v16, 0
	v_sub_f32_e32 v121, v51, v115
	v_cmp_eq_f32_e64 s[76:77], v51, v115
	v_add_f32_dpp v128, v128, v128 row_ror:4 row_mask:0xf bank_mask:0xf
	v_exp_f32_e32 v165, v120
	v_max_f32_dpp v114, v114, v114 row_ror:1 row_mask:0xf bank_mask:0xf
	v_cndmask_b32_e64 v119, v119, 5, s[74:75]
	v_add_f32_dpp v128, v128, v128 row_ror:8 row_mask:0xf bank_mask:0xf
	v_sub_f32_e32 v120, v47, v115
	v_rcp_f32_e32 v244, v128
	v_cmp_eq_f32_e64 s[72:73], v47, v115
	v_pk_mul_f32 v[134:135], v[244:245], v[134:135] op_sel_hi:[0,1]
	v_exp_f32_e32 v164, v121
	v_pk_mul_f32 v[136:137], v[244:245], v[136:137] op_sel_hi:[0,1]
	v_cndmask_b32_e64 v119, v119, 4, s[76:77]
	v_mfma_f32_16x16x4_f32 v[200:203], v133, v15, v[200:203]
	v_sub_f32_e32 v121, v43, v115
	v_max_f32_dpp v114, v114, v114 row_ror:2 row_mask:0xf bank_mask:0xf
	v_cmp_eq_f32_e64 s[74:75], v43, v115
	global_store_dwordx4 v108, v[134:137], s[90:91] sc1
	v_exp_f32_e32 v163, v120
	v_pk_mul_f32 v[138:139], v[244:245], v[138:139] op_sel_hi:[0,1]
	v_cndmask_b32_e64 v119, v119, 3, s[72:73]
	v_pk_mul_f32 v[140:141], v[244:245], v[140:141] op_sel_hi:[0,1]
	v_sub_f32_e32 v120, v39, v115
	v_max_f32_dpp v114, v114, v114 row_ror:4 row_mask:0xf bank_mask:0xf
	v_cmp_eq_f32_e64 s[76:77], v39, v115
	global_store_dwordx4 v108, v[138:141], s[90:91] offset:256 sc1
	v_exp_f32_e32 v162, v121
	v_cndmask_b32_e64 v119, v119, 2, s[74:75]
	v_pk_mul_f32 v[142:143], v[244:245], v[142:143] op_sel_hi:[0,1]
	v_mfma_f32_16x16x4_f32 v[204:207], v133, v17, v[204:207]
	global_load_dwordx4 v[14:17], v104, s[86:87] offset:3072
	v_sub_f32_e32 v121, v35, v115
	v_pk_mul_f32 v[144:145], v[244:245], v[144:145] op_sel_hi:[0,1]
	v_cmp_eq_f32_e64 s[72:73], v35, v115
	global_store_dwordx4 v108, v[142:145], s[90:91] offset:512 sc1
	v_exp_f32_e32 v161, v120
	v_max_f32_dpp v114, v114, v114 row_ror:8 row_mask:0xf bank_mask:0xf
	v_cndmask_b32_e64 v119, v119, 1, s[76:77]
	v_pk_mul_f32 v[146:147], v[244:245], v[146:147] op_sel_hi:[0,1]
	v_exp_f32_e32 v160, v121
	v_pk_mul_f32 v[148:149], v[244:245], v[148:149] op_sel_hi:[0,1]
	v_cndmask_b32_e64 v119, v119, 0, s[72:73]
	global_store_dwordx4 v108, v[146:149], s[90:91] offset:768 sc1
	v_sub_f32_e32 v120, v96, v114
	v_cmp_eq_f32_e64 s[72:73], v96, v114
	s_waitcnt vmcnt(13)
	s_waitcnt vmcnt(27)
	v_mfma_f32_16x16x4_f32 v[208:211], v132, v18, 0
	v_sub_f32_e32 v121, v92, v114
	v_add_u32_e32 v113, s83, v106
	v_cmp_eq_f32_e64 s[74:75], v92, v114
	ds_read2st64_b32 v[250:251], v113 offset1:12
	v_exp_f32_e32 v149, v120
	ds_read2st64_b32 v[252:253], v113 offset0:24 offset1:36
	v_cndmask_b32_e64 v118, v155, 15, s[72:73]
	v_max3_f32 v115, v37, v41, v45
	v_sub_f32_e32 v120, v88, v114
	v_and_b32_e32 v123, 12, v119
	v_cmp_eq_f32_e64 s[76:77], v88, v114
	v_and_b32_e32 v125, 3, v119
	v_exp_f32_e32 v148, v121
	v_add_f32_e32 v129, v160, v161
	v_cndmask_b32_e64 v118, v118, 14, s[74:75]
	v_add_f32_e32 v131, v162, v163
	v_mfma_f32_16x16x4_f32 v[212:215], v132, v20, 0
	v_sub_f32_e32 v121, v84, v114
	v_max3_f32 v117, v49, v53, v57
	v_cmp_eq_f32_e64 s[72:73], v84, v114
	v_lshl_or_b32 v123, v123, 4, v125
	v_exp_f32_e32 v147, v120
	v_cndmask_b32_e64 v118, v118, 13, s[76:77]
	v_add_f32_e32 v129, v129, v164
	v_sub_f32_e32 v120, v80, v114
	v_add_f32_e32 v131, v131, v165
	v_cmp_eq_f32_e64 s[74:75], v80, v114
	v_or_b32_e32 v123, v123, v102
	v_exp_f32_e32 v146, v121
	v_max3_f32 v115, v115, v61, v65
	v_cndmask_b32_e64 v118, v118, 12, s[72:73]
	v_add_f32_e32 v129, v129, v166
	v_mfma_f32_16x16x4_f32 v[208:211], v133, v19, v[208:211]
	v_sub_f32_e32 v121, v76, v114
	v_add_f32_e32 v131, v131, v167
	v_cmp_eq_f32_e64 s[76:77], v76, v114
	v_max_u32_e32 v127, v123, v119
	v_exp_f32_e32 v145, v120
	v_max3_f32 v117, v117, v69, v73
	v_cndmask_b32_e64 v118, v118, 11, s[74:75]
	v_add_f32_e32 v129, v129, v168
	v_sub_f32_e32 v120, v72, v114
	v_add_f32_e32 v131, v131, v169
	v_cmp_eq_f32_e64 s[72:73], v72, v114
	v_min_u32_dpp v127, v127, v127 row_ror:1 row_mask:0xf bank_mask:0xf
	v_exp_f32_e32 v144, v121
	v_add_f32_e32 v129, v129, v170
	v_cndmask_b32_e64 v118, v118, 10, s[76:77]
	v_mfma_f32_16x16x4_f32 v[212:215], v133, v21, v[212:215]
	global_load_dwordx4 v[18:21], v104, s[88:89]
	v_sub_f32_e32 v121, v68, v114
	v_max3_f32 v115, v115, v77, v81
	v_cmp_eq_f32_e64 s[74:75], v68, v114
	v_add_f32_e32 v131, v131, v171
	v_exp_f32_e32 v143, v120
	v_min_u32_dpp v127, v127, v127 row_ror:2 row_mask:0xf bank_mask:0xf
	v_cndmask_b32_e64 v118, v118, 9, s[72:73]
	v_add_f32_e32 v129, v129, v172
	v_sub_f32_e32 v120, v64, v114
	v_max3_f32 v117, v117, v85, v89
	v_cmp_eq_f32_e64 s[76:77], v64, v114
	v_add_f32_e32 v131, v131, v173
	v_exp_f32_e32 v142, v121
	v_min_u32_dpp v127, v127, v127 row_ror:4 row_mask:0xf bank_mask:0xf
	v_cndmask_b32_e64 v118, v118, 8, s[74:75]
	v_add_f32_e32 v129, v129, v174
	s_waitcnt vmcnt(24)
	v_mfma_f32_16x16x4_f32 v[216:219], v132, v22, 0
	v_sub_f32_e32 v121, v60, v114
	v_add_f32_e32 v131, v131, v175
	v_cmp_eq_f32_e64 s[72:73], v60, v114
	v_max3_f32 v115, v115, v93, v97
	v_exp_f32_e32 v141, v120
	v_min_u32_dpp v127, v127, v127 row_ror:8 row_mask:0xf bank_mask:0xf
	v_cndmask_b32_e64 v118, v118, 7, s[76:77]
	v_add_f32_e32 v129, v129, v131
	v_sub_f32_e32 v120, v56, v114
	v_cmp_eq_f32_e64 s[74:75], v56, v114
	v_mad_u32_u24 v249, v127, 24, v107
	v_exp_f32_e32 v140, v121
	v_add_f32_dpp v129, v129, v129 row_ror:1 row_mask:0xf bank_mask:0xf
	v_cndmask_b32_e64 v118, v118, 6, s[72:73]
	v_max_f32_e32 v115, v115, v117
	v_mfma_f32_16x16x4_f32 v[220:223], v132, v24, 0
	v_sub_f32_e32 v121, v52, v114
	global_load_dword v241, v249, s[92:93]
	v_cmp_eq_f32_e64 s[76:77], v52, v114
	v_add_f32_dpp v129, v129, v129 row_ror:2 row_mask:0xf bank_mask:0xf
	v_exp_f32_e32 v139, v120
	s_nop 0
	v_add_f32_dpp v129, v129, v129 row_ror:4 row_mask:0xf bank_mask:0xf
	v_cndmask_b32_e64 v118, v118, 5, s[74:75]
	v_max_f32_dpp v115, v115, v115 row_ror:1 row_mask:0xf bank_mask:0xf
	v_sub_f32_e32 v120, v48, v114
	v_add_f32_dpp v129, v129, v129 row_ror:8 row_mask:0xf bank_mask:0xf
	v_cmp_eq_f32_e64 s[72:73], v48, v114
	v_rcp_f32_e32 v246, v129
	v_exp_f32_e32 v138, v121
	v_pk_mul_f32 v[160:161], v[246:247], v[160:161] op_sel_hi:[0,1]
	v_cndmask_b32_e64 v118, v118, 4, s[76:77]
	v_pk_mul_f32 v[162:163], v[246:247], v[162:163] op_sel_hi:[0,1]
	v_mfma_f32_16x16x4_f32 v[216:219], v133, v23, v[216:219]
	v_sub_f32_e32 v121, v44, v114
	v_max_f32_dpp v115, v115, v115 row_ror:2 row_mask:0xf bank_mask:0xf
	v_cmp_eq_f32_e64 s[74:75], v44, v114
	v_exp_f32_e32 v137, v120
	global_store_dwordx4 v109, v[160:163], s[90:91] sc1
	v_cndmask_b32_e64 v118, v118, 3, s[72:73]
	v_pk_mul_f32 v[164:165], v[246:247], v[164:165] op_sel_hi:[0,1]
	v_sub_f32_e32 v120, v40, v114
	v_pk_mul_f32 v[166:167], v[246:247], v[166:167] op_sel_hi:[0,1]
	v_cmp_eq_f32_e64 s[76:77], v40, v114
	v_max_f32_dpp v115, v115, v115 row_ror:4 row_mask:0xf bank_mask:0xf
	v_exp_f32_e32 v136, v121
	global_store_dwordx4 v109, v[164:167], s[90:91] offset:256 sc1
	v_cndmask_b32_e64 v118, v118, 2, s[74:75]
	v_pk_mul_f32 v[168:169], v[246:247], v[168:169] op_sel_hi:[0,1]
	v_mfma_f32_16x16x4_f32 v[220:223], v133, v25, v[220:223]
	global_load_dwordx4 v[22:25], v104, s[88:89] offset:1024
	v_sub_f32_e32 v121, v36, v114
	v_pk_mul_f32 v[170:171], v[246:247], v[170:171] op_sel_hi:[0,1]
	v_cmp_eq_f32_e64 s[72:73], v36, v114
	global_store_dwordx4 v109, v[168:171], s[90:91] offset:512 sc1
	v_exp_f32_e32 v135, v120
	v_max_f32_dpp v115, v115, v115 row_ror:8 row_mask:0xf bank_mask:0xf
	v_cndmask_b32_e64 v118, v118, 1, s[76:77]
	v_pk_mul_f32 v[172:173], v[246:247], v[172:173] op_sel_hi:[0,1]
	v_exp_f32_e32 v134, v121
	v_pk_mul_f32 v[174:175], v[246:247], v[174:175] op_sel_hi:[0,1]
	v_cndmask_b32_e64 v118, v118, 0, s[72:73]
	global_store_dwordx4 v109, v[172:175], s[90:91] offset:768 sc1
	v_sub_f32_e32 v120, v97, v115
	v_cmp_eq_f32_e64 s[72:73], v97, v115
	s_waitcnt lgkmcnt(0)
	s_waitcnt vmcnt(27)
	v_mfma_f32_16x16x4_f32 v[224:227], v132, v26, 0
	v_sub_f32_e32 v121, v93, v115
	v_add_f32_e32 v250, v159, v250
	v_cmp_eq_f32_e64 s[74:75], v93, v115
	v_add_f32_e32 v251, v158, v251
	v_exp_f32_e32 v175, v120
	v_cndmask_b32_e64 v119, v155, 15, s[72:73]
	v_add_f32_e32 v252, v157, v252
	v_sub_f32_e32 v120, v89, v115
	v_add_f32_e32 v253, v156, v253
	v_cmp_eq_f32_e64 s[76:77], v89, v115
	ds_write2st64_b32 v113, v250, v251 offset1:12
	v_exp_f32_e32 v174, v121
	ds_write2st64_b32 v113, v252, v253 offset0:24 offset1:36
	v_cndmask_b32_e64 v119, v119, 14, s[74:75]
	v_mfma_f32_16x16x4_f32 v[228:231], v132, v28, 0
	v_sub_f32_e32 v121, v85, v115
	v_and_b32_e32 v122, 12, v118
	v_cmp_eq_f32_e64 s[72:73], v85, v115
	v_and_b32_e32 v124, 3, v118
	v_exp_f32_e32 v173, v120
	v_add_f32_e32 v128, v134, v135
	v_cndmask_b32_e64 v119, v119, 13, s[76:77]
	v_sub_f32_e32 v120, v81, v115
	v_add_f32_e32 v130, v136, v137
	v_cmp_eq_f32_e64 s[74:75], v81, v115
	v_lshl_or_b32 v122, v122, 4, v124
	v_exp_f32_e32 v172, v121
	v_add_f32_e32 v128, v128, v138
	v_cndmask_b32_e64 v119, v119, 12, s[72:73]
	v_add_f32_e32 v130, v130, v139
	v_mfma_f32_16x16x4_f32 v[224:227], v133, v27, v[224:227]
	v_sub_f32_e32 v121, v77, v115
	v_cmp_eq_f32_e64 s[76:77], v77, v115
	v_or_b32_e32 v122, v122, v102
	v_exp_f32_e32 v171, v120
	v_add_f32_e32 v128, v128, v140
	v_cndmask_b32_e64 v119, v119, 11, s[74:75]
	v_add_f32_e32 v130, v130, v141
	v_sub_f32_e32 v120, v73, v115
	v_cmp_eq_f32_e64 s[72:73], v73, v115
	v_max_u32_e32 v126, v122, v118
	v_exp_f32_e32 v170, v121
	v_add_f32_e32 v128, v128, v142
	v_cndmask_b32_e64 v119, v119, 10, s[76:77]
	v_add_f32_e32 v130, v130, v143
	v_mfma_f32_16x16x4_f32 v[228:231], v133, v29, v[228:231]
	global_load_dwordx4 v[26:29], v104, s[88:89] offset:2048
	v_sub_f32_e32 v121, v69, v115
	v_min_u32_dpp v126, v126, v126 row_ror:1 row_mask:0xf bank_mask:0xf
	v_cmp_eq_f32_e64 s[74:75], v69, v115
	v_exp_f32_e32 v169, v120
	v_add_f32_e32 v128, v128, v144
	v_cndmask_b32_e64 v119, v119, 9, s[72:73]
	v_add_f32_e32 v130, v130, v145
	v_sub_f32_e32 v120, v65, v115
	v_min_u32_dpp v126, v126, v126 row_ror:2 row_mask:0xf bank_mask:0xf
	v_cmp_eq_f32_e64 s[76:77], v65, v115
	v_add_f32_e32 v128, v128, v146
	v_exp_f32_e32 v168, v121
	v_cndmask_b32_e64 v119, v119, 8, s[74:75]
	v_add_f32_e32 v130, v130, v147
	s_waitcnt vmcnt(24)
	v_mfma_f32_16x16x4_f32 v[232:235], v132, v30, 0
	v_sub_f32_e32 v121, v61, v115
	v_min_u32_dpp v126, v126, v126 row_ror:4 row_mask:0xf bank_mask:0xf
	v_cmp_eq_f32_e64 s[72:73], v61, v115
	v_add_f32_e32 v128, v128, v148
	v_exp_f32_e32 v167, v120
	v_cndmask_b32_e64 v119, v119, 7, s[76:77]
	v_add_f32_e32 v130, v130, v149
	v_sub_f32_e32 v120, v57, v115
	v_min_u32_dpp v126, v126, v126 row_ror:8 row_mask:0xf bank_mask:0xf
	v_cmp_eq_f32_e64 s[74:75], v57, v115
	v_add_f32_e32 v128, v128, v130
	v_exp_f32_e32 v166, v121
	v_mad_u32_u24 v248, v126, 24, v107
	v_cndmask_b32_e64 v119, v119, 6, s[72:73]
	v_mfma_f32_16x16x4_f32 v[236:239], v132, v32, 0
	v_sub_f32_e32 v121, v53, v115
	v_add_f32_dpp v128, v128, v128 row_ror:1 row_mask:0xf bank_mask:0xf
	v_cmp_eq_f32_e64 s[76:77], v53, v115
	global_load_dword v242, v248, s[92:93]
	v_exp_f32_e32 v165, v120
	v_add_f32_dpp v128, v128, v128 row_ror:2 row_mask:0xf bank_mask:0xf
	v_cndmask_b32_e64 v119, v119, 5, s[74:75]
	v_sub_f32_e32 v120, v49, v115
	v_add_f32_dpp v128, v128, v128 row_ror:4 row_mask:0xf bank_mask:0xf
	v_cmp_eq_f32_e64 s[72:73], v49, v115
	s_nop 0
	v_add_f32_dpp v128, v128, v128 row_ror:8 row_mask:0xf bank_mask:0xf
	v_exp_f32_e32 v164, v121
	v_rcp_f32_e32 v244, v128
	v_cndmask_b32_e64 v119, v119, 4, s[76:77]
	v_pk_mul_f32 v[134:135], v[244:245], v[134:135] op_sel_hi:[0,1]
	v_mfma_f32_16x16x4_f32 v[232:235], v133, v31, v[232:235]
	v_sub_f32_e32 v121, v45, v115
	v_cmp_eq_f32_e64 s[74:75], v45, v115
	v_pk_mul_f32 v[136:137], v[244:245], v[136:137] op_sel_hi:[0,1]
	v_exp_f32_e32 v163, v120
	global_store_dwordx4 v110, v[134:137], s[90:91] sc1
	v_cndmask_b32_e64 v119, v119, 3, s[72:73]
	v_pk_mul_f32 v[138:139], v[244:245], v[138:139] op_sel_hi:[0,1]
	v_sub_f32_e32 v120, v41, v115
	v_cmp_eq_f32_e64 s[76:77], v41, v115
	v_pk_mul_f32 v[140:141], v[244:245], v[140:141] op_sel_hi:[0,1]
	v_exp_f32_e32 v162, v121
	global_store_dwordx4 v110, v[138:141], s[90:91] offset:256 sc1
	v_cndmask_b32_e64 v119, v119, 2, s[74:75]
	v_pk_mul_f32 v[142:143], v[244:245], v[142:143] op_sel_hi:[0,1]
	v_mfma_f32_16x16x4_f32 v[236:239], v133, v33, v[236:239]
	global_load_dwordx4 v[30:33], v104, s[88:89] offset:3072
	v_sub_f32_e32 v121, v37, v115
	v_pk_mul_f32 v[144:145], v[244:245], v[144:145] op_sel_hi:[0,1]
	v_cmp_eq_f32_e64 s[72:73], v37, v115
	v_exp_f32_e32 v161, v120
	global_store_dwordx4 v110, v[142:145], s[90:91] offset:512 sc1
	v_cndmask_b32_e64 v119, v119, 1, s[76:77]
	v_pk_mul_f32 v[146:147], v[244:245], v[146:147] op_sel_hi:[0,1]
	v_exp_f32_e32 v160, v121
	v_pk_mul_f32 v[148:149], v[244:245], v[148:149] op_sel_hi:[0,1]
	v_cndmask_b32_e64 v119, v119, 0, s[72:73]
	global_store_dwordx4 v110, v[146:149], s[90:91] offset:768 sc1
	v_and_b32_e32 v123, 12, v119
	v_max3_f32 v114, v176, v180, v184
	v_and_b32_e32 v125, 3, v119
	v_add_f32_e32 v129, v160, v161
	v_add_f32_e32 v131, v162, v163
	v_max3_f32 v116, v188, v192, v196
	v_lshl_or_b32 v123, v123, 4, v125
	v_add_f32_e32 v129, v129, v164
	v_add_f32_e32 v131, v131, v165
	v_or_b32_e32 v123, v123, v102
	v_max3_f32 v114, v114, v200, v204
	v_add_f32_e32 v129, v129, v166
	v_add_f32_e32 v131, v131, v167
	v_max_u32_e32 v127, v123, v119
	v_max3_f32 v116, v116, v208, v212
	v_add_f32_e32 v129, v129, v168
	v_add_f32_e32 v131, v131, v169
	v_min_u32_dpp v127, v127, v127 row_ror:1 row_mask:0xf bank_mask:0xf
	v_add_f32_e32 v129, v129, v170
	v_max3_f32 v114, v114, v216, v220
	v_add_f32_e32 v131, v131, v171
	v_min_u32_dpp v127, v127, v127 row_ror:2 row_mask:0xf bank_mask:0xf
	v_add_f32_e32 v129, v129, v172
	v_max3_f32 v116, v116, v224, v228
	v_add_f32_e32 v131, v131, v173
	v_min_u32_dpp v127, v127, v127 row_ror:4 row_mask:0xf bank_mask:0xf
	v_add_f32_e32 v129, v129, v174
	v_add_f32_e32 v131, v131, v175
	v_max3_f32 v114, v114, v232, v236
	v_min_u32_dpp v127, v127, v127 row_ror:8 row_mask:0xf bank_mask:0xf
	v_add_f32_e32 v129, v129, v131
	v_mad_u32_u24 v249, v127, 24, v107
	s_nop 0
	v_add_f32_dpp v129, v129, v129 row_ror:1 row_mask:0xf bank_mask:0xf
	v_max_f32_e32 v114, v114, v116
	global_load_dword v243, v249, s[92:93]
	v_add_f32_dpp v129, v129, v129 row_ror:2 row_mask:0xf bank_mask:0xf
	s_nop 1
	v_add_f32_dpp v129, v129, v129 row_ror:4 row_mask:0xf bank_mask:0xf
	v_max_f32_dpp v114, v114, v114 row_ror:1 row_mask:0xf bank_mask:0xf
	s_nop 0
	v_add_f32_dpp v129, v129, v129 row_ror:8 row_mask:0xf bank_mask:0xf
	v_rcp_f32_e32 v246, v129
	s_nop 0
	v_pk_mul_f32 v[160:161], v[246:247], v[160:161] op_sel_hi:[0,1]
	v_pk_mul_f32 v[162:163], v[246:247], v[162:163] op_sel_hi:[0,1]
	v_max_f32_dpp v114, v114, v114 row_ror:2 row_mask:0xf bank_mask:0xf
	global_store_dwordx4 v111, v[160:163], s[90:91] sc1
	v_pk_mul_f32 v[164:165], v[246:247], v[164:165] op_sel_hi:[0,1]
	v_pk_mul_f32 v[166:167], v[246:247], v[166:167] op_sel_hi:[0,1]
	v_max_f32_dpp v114, v114, v114 row_ror:4 row_mask:0xf bank_mask:0xf
	global_store_dwordx4 v111, v[164:167], s[90:91] offset:256 sc1
	v_pk_mul_f32 v[168:169], v[246:247], v[168:169] op_sel_hi:[0,1]
	v_pk_mul_f32 v[170:171], v[246:247], v[170:171] op_sel_hi:[0,1]
	global_store_dwordx4 v111, v[168:171], s[90:91] offset:512 sc1
	v_max_f32_dpp v114, v114, v114 row_ror:8 row_mask:0xf bank_mask:0xf
	v_pk_mul_f32 v[172:173], v[246:247], v[172:173] op_sel_hi:[0,1]
	v_pk_mul_f32 v[174:175], v[246:247], v[174:175] op_sel_hi:[0,1]
	global_store_dwordx4 v111, v[172:175], s[90:91] offset:768 sc1
	s_add_i32 s70, s70, 1
	s_waitcnt lgkmcnt(0)
	s_lshl_b32 s84, s70, 13
	s_add_u32 s90, s80, s84
	s_addc_u32 s91, s81, 0
	s_mul_i32 s84, s70, 0xc000
	s_add_u32 s92, s94, s84
	s_addc_u32 s93, s95, 0
	s_add_i32 s84, s70, 2
	s_and_b32 s84, s84, 15
	s_lshl_b32 s82, s84, 12
	s_lshl_b32 s84, s84, 16
	s_add_u32 s84, s84, 0x787000
	s_add_u32 s86, s40, s84
	s_addc_u32 s87, s41, 0
	s_add_u32 s88, s86, 0x1000
	s_addc_u32 s89, s87, 0
	s_add_i32 s84, s70, 15
	s_and_b32 s84, s84, 15
	s_mul_i32 s84, s84, 0xc0
	s_add_u32 s83, s84, 0x10000
	v_add_u32_e32 v112, s82, v105
	v_sub_f32_e32 v120, v236, v114
	v_cmp_eq_f32_e64 s[72:73], v236, v114
	s_waitcnt vmcnt(27)
	v_mfma_f32_16x16x4_f32 v[34:37], v254, v6, 0
	ds_read2st64_b32 v[132:133], v112 offset1:1
	v_sub_f32_e32 v121, v232, v114
	v_cmp_eq_f32_e64 s[74:75], v232, v114
	v_exp_f32_e32 v149, v120
	v_cndmask_b32_e64 v118, v155, 15, s[72:73]
	v_max3_f32 v115, v177, v181, v185
	v_sub_f32_e32 v120, v228, v114
	v_cmp_eq_f32_e64 s[76:77], v228, v114
	v_exp_f32_e32 v148, v121
	v_cndmask_b32_e64 v118, v118, 14, s[74:75]
	v_mfma_f32_16x16x4_f32 v[38:41], v254, v8, 0
	v_sub_f32_e32 v121, v224, v114
	v_max3_f32 v117, v189, v193, v197
	v_cmp_eq_f32_e64 s[72:73], v224, v114
	v_exp_f32_e32 v147, v120
	v_cndmask_b32_e64 v118, v118, 13, s[76:77]
	v_sub_f32_e32 v120, v220, v114
	v_cmp_eq_f32_e64 s[74:75], v220, v114
	v_max3_f32 v115, v115, v201, v205
	v_exp_f32_e32 v146, v121
	v_cndmask_b32_e64 v118, v118, 12, s[72:73]
	v_mfma_f32_16x16x4_f32 v[34:37], v255, v7, v[34:37]
	v_sub_f32_e32 v121, v216, v114
	v_cmp_eq_f32_e64 s[76:77], v216, v114
	v_exp_f32_e32 v145, v120
	v_cndmask_b32_e64 v118, v118, 11, s[74:75]
	v_max3_f32 v117, v117, v209, v213
	v_sub_f32_e32 v120, v212, v114
	v_cmp_eq_f32_e64 s[72:73], v212, v114
	v_exp_f32_e32 v144, v121
	v_cndmask_b32_e64 v118, v118, 10, s[76:77]
	v_mfma_f32_16x16x4_f32 v[38:41], v255, v9, v[38:41]
	global_load_dwordx4 v[6:9], v104, s[86:87]
	v_sub_f32_e32 v121, v208, v114
	v_max3_f32 v115, v115, v217, v221
	v_cmp_eq_f32_e64 s[74:75], v208, v114
	v_exp_f32_e32 v143, v120
	v_cndmask_b32_e64 v118, v118, 9, s[72:73]
	v_sub_f32_e32 v120, v204, v114
	v_cmp_eq_f32_e64 s[76:77], v204, v114
	v_max3_f32 v117, v117, v225, v229
	v_exp_f32_e32 v142, v121
	v_cndmask_b32_e64 v118, v118, 8, s[74:75]
	s_waitcnt vmcnt(27)
	v_mfma_f32_16x16x4_f32 v[42:45], v254, v2, 0
	v_sub_f32_e32 v121, v200, v114
	v_cmp_eq_f32_e64 s[72:73], v200, v114
	v_exp_f32_e32 v141, v120
	v_cndmask_b32_e64 v118, v118, 7, s[76:77]
	v_max3_f32 v115, v115, v233, v237
	v_sub_f32_e32 v120, v196, v114
	v_cmp_eq_f32_e64 s[74:75], v196, v114
	v_exp_f32_e32 v140, v121
	v_cndmask_b32_e64 v118, v118, 6, s[72:73]
	v_mfma_f32_16x16x4_f32 v[46:49], v254, v4, 0
	v_sub_f32_e32 v121, v192, v114
	v_max_f32_e32 v115, v115, v117
	v_cmp_eq_f32_e64 s[76:77], v192, v114
	v_exp_f32_e32 v139, v120
	v_cndmask_b32_e64 v118, v118, 5, s[74:75]
	v_sub_f32_e32 v120, v188, v114
	v_cmp_eq_f32_e64 s[72:73], v188, v114
	v_max_f32_dpp v115, v115, v115 row_ror:1 row_mask:0xf bank_mask:0xf
	v_exp_f32_e32 v138, v121
	v_cndmask_b32_e64 v118, v118, 4, s[76:77]
	v_mfma_f32_16x16x4_f32 v[42:45], v255, v3, v[42:45]
	v_sub_f32_e32 v121, v184, v114
	v_cmp_eq_f32_e64 s[74:75], v184, v114
	v_exp_f32_e32 v137, v120
	v_cndmask_b32_e64 v118, v118, 3, s[72:73]
	v_max_f32_dpp v115, v115, v115 row_ror:2 row_mask:0xf bank_mask:0xf
	v_sub_f32_e32 v120, v180, v114
	v_cmp_eq_f32_e64 s[76:77], v180, v114
	v_exp_f32_e32 v136, v121
	v_cndmask_b32_e64 v118, v118, 2, s[74:75]
	v_mfma_f32_16x16x4_f32 v[46:49], v255, v5, v[46:49]
	global_load_dwordx4 v[2:5], v104, s[86:87] offset:1024
	v_sub_f32_e32 v121, v176, v114
	v_max_f32_dpp v115, v115, v115 row_ror:4 row_mask:0xf bank_mask:0xf
	v_cmp_eq_f32_e64 s[72:73], v176, v114
	v_exp_f32_e32 v135, v120
	v_cndmask_b32_e64 v118, v118, 1, s[76:77]
	v_exp_f32_e32 v134, v121
	v_cndmask_b32_e64 v118, v118, 0, s[72:73]
	v_max_f32_dpp v115, v115, v115 row_ror:8 row_mask:0xf bank_mask:0xf
	v_sub_f32_e32 v120, v237, v115
	v_cmp_eq_f32_e64 s[72:73], v237, v115
	v_max3_f32 v114, v178, v182, v186
	s_waitcnt vmcnt(27)
	v_mfma_f32_16x16x4_f32 v[50:53], v254, v10, 0
	v_sub_f32_e32 v121, v233, v115
	v_and_b32_e32 v122, 12, v118
	v_cmp_eq_f32_e64 s[74:75], v233, v115
	v_and_b32_e32 v124, 3, v118
	v_exp_f32_e32 v175, v120
	v_add_f32_e32 v128, v134, v135
	v_cndmask_b32_e64 v119, v155, 15, s[72:73]
	v_add_f32_e32 v130, v136, v137
	v_sub_f32_e32 v120, v229, v115
	v_max3_f32 v116, v190, v194, v198
	v_cmp_eq_f32_e64 s[76:77], v229, v115
	v_exp_f32_e32 v174, v121
	v_lshl_or_b32 v122, v122, 4, v124
	v_cndmask_b32_e64 v119, v119, 14, s[74:75]
	v_add_f32_e32 v128, v128, v138
	v_mfma_f32_16x16x4_f32 v[54:57], v254, v12, 0
	v_sub_f32_e32 v121, v225, v115
	v_add_f32_e32 v130, v130, v139
	v_cmp_eq_f32_e64 s[72:73], v225, v115
	v_or_b32_e32 v122, v122, v102
	v_exp_f32_e32 v173, v120
	v_max3_f32 v114, v114, v202, v206
	v_cndmask_b32_e64 v119, v119, 13, s[76:77]
	v_add_f32_e32 v128, v128, v140
	v_sub_f32_e32 v120, v221, v115
	v_cmp_eq_f32_e64 s[74:75], v221, v115
	v_add_f32_e32 v130, v130, v141
	v_exp_f32_e32 v172, v121
	v_max_u32_e32 v126, v122, v118
	v_cndmask_b32_e64 v119, v119, 12, s[72:73]
	v_max3_f32 v116, v116, v210, v214
	v_mfma_f32_16x16x4_f32 v[50:53], v255, v11, v[50:53]
	v_sub_f32_e32 v121, v217, v115
	v_add_f32_e32 v128, v128, v142
	v_cmp_eq_f32_e64 s[76:77], v217, v115
	v_add_f32_e32 v130, v130, v143
	v_exp_f32_e32 v171, v120
	v_min_u32_dpp v126, v126, v126 row_ror:1 row_mask:0xf bank_mask:0xf
	v_cndmask_b32_e64 v119, v119, 11, s[74:75]
	v_sub_f32_e32 v120, v213, v115
	v_add_f32_e32 v128, v128, v144
	v_cmp_eq_f32_e64 s[72:73], v213, v115
	v_max3_f32 v114, v114, v218, v222
	v_exp_f32_e32 v170, v121
	v_add_f32_e32 v130, v130, v145
	v_cndmask_b32_e64 v119, v119, 10, s[76:77]
	v_min_u32_dpp v126, v126, v126 row_ror:2 row_mask:0xf bank_mask:0xf
	v_mfma_f32_16x16x4_f32 v[54:57], v255, v13, v[54:57]
	global_load_dwordx4 v[10:13], v104, s[86:87] offset:2048
	v_sub_f32_e32 v121, v209, v115
	v_add_f32_e32 v128, v128, v146
	v_cmp_eq_f32_e64 s[74:75], v209, v115
	v_max3_f32 v116, v116, v226, v230
	v_exp_f32_e32 v169, v120
	v_cndmask_b32_e64 v119, v119, 9, s[72:73]
	v_add_f32_e32 v130, v130, v147
	v_sub_f32_e32 v120, v205, v115
	v_min_u32_dpp v126, v126, v126 row_ror:4 row_mask:0xf bank_mask:0xf
	v_cmp_eq_f32_e64 s[76:77], v205, v115
	v_add_f32_e32 v128, v128, v148
	v_exp_f32_e32 v168, v121
	v_add_f32_e32 v130, v130, v149
	v_cndmask_b32_e64 v119, v119, 8, s[74:75]
	v_max3_f32 v114, v114, v234, v238
	s_waitcnt vmcnt(24)
	v_mfma_f32_16x16x4_f32 v[58:61], v254, v14, 0
	v_sub_f32_e32 v121, v201, v115
	v_min_u32_dpp v126, v126, v126 row_ror:8 row_mask:0xf bank_mask:0xf
	v_cmp_eq_f32_e64 s[72:73], v201, v115
	v_exp_f32_e32 v167, v120
	v_add_f32_e32 v128, v128, v130
	v_cndmask_b32_e64 v119, v119, 7, s[76:77]
	v_mad_u32_u24 v248, v126, 24, v107
	v_sub_f32_e32 v120, v197, v115
	v_add_f32_dpp v128, v128, v128 row_ror:1 row_mask:0xf bank_mask:0xf
	v_cmp_eq_f32_e64 s[74:75], v197, v115
	v_max_f32_e32 v114, v114, v116
	v_exp_f32_e32 v166, v121
	global_load_dword v159, v248, s[92:93]
	v_cndmask_b32_e64 v119, v119, 6, s[72:73]
	v_add_f32_dpp v128, v128, v128 row_ror:2 row_mask:0xf bank_mask:0xf
	v_mfma_f32_16x16x4_f32 v[62:65], v254, v16, 0
	v_sub_f32_e32 v121, v193, v115
	v_cmp_eq_f32_e64 s[76:77], v193, v115
	v_add_f32_dpp v128, v128, v128 row_ror:4 row_mask:0xf bank_mask:0xf
	v_exp_f32_e32 v165, v120
	v_max_f32_dpp v114, v114, v114 row_ror:1 row_mask:0xf bank_mask:0xf
	v_cndmask_b32_e64 v119, v119, 5, s[74:75]
	v_add_f32_dpp v128, v128, v128 row_ror:8 row_mask:0xf bank_mask:0xf
	v_sub_f32_e32 v120, v189, v115
	v_rcp_f32_e32 v244, v128
	v_cmp_eq_f32_e64 s[72:73], v189, v115
	v_pk_mul_f32 v[134:135], v[244:245], v[134:135] op_sel_hi:[0,1]
	v_exp_f32_e32 v164, v121
	v_pk_mul_f32 v[136:137], v[244:245], v[136:137] op_sel_hi:[0,1]
	v_cndmask_b32_e64 v119, v119, 4, s[76:77]
	v_mfma_f32_16x16x4_f32 v[58:61], v255, v15, v[58:61]
	v_sub_f32_e32 v121, v185, v115
	v_max_f32_dpp v114, v114, v114 row_ror:2 row_mask:0xf bank_mask:0xf
	v_cmp_eq_f32_e64 s[74:75], v185, v115
	global_store_dwordx4 v108, v[134:137], s[90:91] sc1
	v_exp_f32_e32 v163, v120
	v_pk_mul_f32 v[138:139], v[244:245], v[138:139] op_sel_hi:[0,1]
	v_cndmask_b32_e64 v119, v119, 3, s[72:73]
	v_pk_mul_f32 v[140:141], v[244:245], v[140:141] op_sel_hi:[0,1]
	v_sub_f32_e32 v120, v181, v115
	v_max_f32_dpp v114, v114, v114 row_ror:4 row_mask:0xf bank_mask:0xf
	v_cmp_eq_f32_e64 s[76:77], v181, v115
	global_store_dwordx4 v108, v[138:141], s[90:91] offset:256 sc1
	v_exp_f32_e32 v162, v121
	v_cndmask_b32_e64 v119, v119, 2, s[74:75]
	v_pk_mul_f32 v[142:143], v[244:245], v[142:143] op_sel_hi:[0,1]
	v_mfma_f32_16x16x4_f32 v[62:65], v255, v17, v[62:65]
	global_load_dwordx4 v[14:17], v104, s[86:87] offset:3072
	v_sub_f32_e32 v121, v177, v115
	v_pk_mul_f32 v[144:145], v[244:245], v[144:145] op_sel_hi:[0,1]
	v_cmp_eq_f32_e64 s[72:73], v177, v115
	global_store_dwordx4 v108, v[142:145], s[90:91] offset:512 sc1
	v_exp_f32_e32 v161, v120
	v_max_f32_dpp v114, v114, v114 row_ror:8 row_mask:0xf bank_mask:0xf
	v_cndmask_b32_e64 v119, v119, 1, s[76:77]
	v_pk_mul_f32 v[146:147], v[244:245], v[146:147] op_sel_hi:[0,1]
	v_exp_f32_e32 v160, v121
	v_pk_mul_f32 v[148:149], v[244:245], v[148:149] op_sel_hi:[0,1]
	v_cndmask_b32_e64 v119, v119, 0, s[72:73]
	global_store_dwordx4 v108, v[146:149], s[90:91] offset:768 sc1
	v_sub_f32_e32 v120, v238, v114
	v_cmp_eq_f32_e64 s[72:73], v238, v114
	s_waitcnt vmcnt(13)
	s_waitcnt vmcnt(27)
	v_mfma_f32_16x16x4_f32 v[66:69], v254, v18, 0
	v_sub_f32_e32 v121, v234, v114
	v_add_u32_e32 v113, s83, v106
	v_cmp_eq_f32_e64 s[74:75], v234, v114
	ds_read2st64_b32 v[250:251], v113 offset1:12
	v_exp_f32_e32 v149, v120
	ds_read2st64_b32 v[252:253], v113 offset0:24 offset1:36
	v_cndmask_b32_e64 v118, v155, 15, s[72:73]
	v_max3_f32 v115, v179, v183, v187
	v_sub_f32_e32 v120, v230, v114
	v_and_b32_e32 v123, 12, v119
	v_cmp_eq_f32_e64 s[76:77], v230, v114
	v_and_b32_e32 v125, 3, v119
	v_exp_f32_e32 v148, v121
	v_add_f32_e32 v129, v160, v161
	v_cndmask_b32_e64 v118, v118, 14, s[74:75]
	v_add_f32_e32 v131, v162, v163
	v_mfma_f32_16x16x4_f32 v[70:73], v254, v20, 0
	v_sub_f32_e32 v121, v226, v114
	v_max3_f32 v117, v191, v195, v199
	v_cmp_eq_f32_e64 s[72:73], v226, v114
	v_lshl_or_b32 v123, v123, 4, v125
	v_exp_f32_e32 v147, v120
	v_cndmask_b32_e64 v118, v118, 13, s[76:77]
	v_add_f32_e32 v129, v129, v164
	v_sub_f32_e32 v120, v222, v114
	v_add_f32_e32 v131, v131, v165
	v_cmp_eq_f32_e64 s[74:75], v222, v114
	v_or_b32_e32 v123, v123, v102
	v_exp_f32_e32 v146, v121
	v_max3_f32 v115, v115, v203, v207
	v_cndmask_b32_e64 v118, v118, 12, s[72:73]
	v_add_f32_e32 v129, v129, v166
	v_mfma_f32_16x16x4_f32 v[66:69], v255, v19, v[66:69]
	v_sub_f32_e32 v121, v218, v114
	v_add_f32_e32 v131, v131, v167
	v_cmp_eq_f32_e64 s[76:77], v218, v114
	v_max_u32_e32 v127, v123, v119
	v_exp_f32_e32 v145, v120
	v_max3_f32 v117, v117, v211, v215
	v_cndmask_b32_e64 v118, v118, 11, s[74:75]
	v_add_f32_e32 v129, v129, v168
	v_sub_f32_e32 v120, v214, v114
	v_add_f32_e32 v131, v131, v169
	v_cmp_eq_f32_e64 s[72:73], v214, v114
	v_min_u32_dpp v127, v127, v127 row_ror:1 row_mask:0xf bank_mask:0xf
	v_exp_f32_e32 v144, v121
	v_add_f32_e32 v129, v129, v170
	v_cndmask_b32_e64 v118, v118, 10, s[76:77]
	v_mfma_f32_16x16x4_f32 v[70:73], v255, v21, v[70:73]
	global_load_dwordx4 v[18:21], v104, s[88:89]
	v_sub_f32_e32 v121, v210, v114
	v_max3_f32 v115, v115, v219, v223
	v_cmp_eq_f32_e64 s[74:75], v210, v114
	v_add_f32_e32 v131, v131, v171
	v_exp_f32_e32 v143, v120
	v_min_u32_dpp v127, v127, v127 row_ror:2 row_mask:0xf bank_mask:0xf
	v_cndmask_b32_e64 v118, v118, 9, s[72:73]
	v_add_f32_e32 v129, v129, v172
	v_sub_f32_e32 v120, v206, v114
	v_max3_f32 v117, v117, v227, v231
	v_cmp_eq_f32_e64 s[76:77], v206, v114
	v_add_f32_e32 v131, v131, v173
	v_exp_f32_e32 v142, v121
	v_min_u32_dpp v127, v127, v127 row_ror:4 row_mask:0xf bank_mask:0xf
	v_cndmask_b32_e64 v118, v118, 8, s[74:75]
	v_add_f32_e32 v129, v129, v174
	s_waitcnt vmcnt(24)
	v_mfma_f32_16x16x4_f32 v[74:77], v254, v22, 0
	v_sub_f32_e32 v121, v202, v114
	v_add_f32_e32 v131, v131, v175
	v_cmp_eq_f32_e64 s[72:73], v202, v114
	v_max3_f32 v115, v115, v235, v239
	v_exp_f32_e32 v141, v120
	v_min_u32_dpp v127, v127, v127 row_ror:8 row_mask:0xf bank_mask:0xf
	v_cndmask_b32_e64 v118, v118, 7, s[76:77]
	v_add_f32_e32 v129, v129, v131
	v_sub_f32_e32 v120, v198, v114
	v_cmp_eq_f32_e64 s[74:75], v198, v114
	v_mad_u32_u24 v249, v127, 24, v107
	v_exp_f32_e32 v140, v121
	v_add_f32_dpp v129, v129, v129 row_ror:1 row_mask:0xf bank_mask:0xf
	v_cndmask_b32_e64 v118, v118, 6, s[72:73]
	v_max_f32_e32 v115, v115, v117
	v_mfma_f32_16x16x4_f32 v[78:81], v254, v24, 0
	v_sub_f32_e32 v121, v194, v114
	global_load_dword v158, v249, s[92:93]
	v_cmp_eq_f32_e64 s[76:77], v194, v114
	v_add_f32_dpp v129, v129, v129 row_ror:2 row_mask:0xf bank_mask:0xf
	v_exp_f32_e32 v139, v120
	s_nop 0
	v_add_f32_dpp v129, v129, v129 row_ror:4 row_mask:0xf bank_mask:0xf
	v_cndmask_b32_e64 v118, v118, 5, s[74:75]
	v_max_f32_dpp v115, v115, v115 row_ror:1 row_mask:0xf bank_mask:0xf
	v_sub_f32_e32 v120, v190, v114
	v_add_f32_dpp v129, v129, v129 row_ror:8 row_mask:0xf bank_mask:0xf
	v_cmp_eq_f32_e64 s[72:73], v190, v114
	v_rcp_f32_e32 v246, v129
	v_exp_f32_e32 v138, v121
	v_pk_mul_f32 v[160:161], v[246:247], v[160:161] op_sel_hi:[0,1]
	v_cndmask_b32_e64 v118, v118, 4, s[76:77]
	v_pk_mul_f32 v[162:163], v[246:247], v[162:163] op_sel_hi:[0,1]
	v_mfma_f32_16x16x4_f32 v[74:77], v255, v23, v[74:77]
	v_sub_f32_e32 v121, v186, v114
	v_max_f32_dpp v115, v115, v115 row_ror:2 row_mask:0xf bank_mask:0xf
	v_cmp_eq_f32_e64 s[74:75], v186, v114
	v_exp_f32_e32 v137, v120
	global_store_dwordx4 v109, v[160:163], s[90:91] sc1
	v_cndmask_b32_e64 v118, v118, 3, s[72:73]
	v_pk_mul_f32 v[164:165], v[246:247], v[164:165] op_sel_hi:[0,1]
	v_sub_f32_e32 v120, v182, v114
	v_pk_mul_f32 v[166:167], v[246:247], v[166:167] op_sel_hi:[0,1]
	v_cmp_eq_f32_e64 s[76:77], v182, v114
	v_max_f32_dpp v115, v115, v115 row_ror:4 row_mask:0xf bank_mask:0xf
	v_exp_f32_e32 v136, v121
	global_store_dwordx4 v109, v[164:167], s[90:91] offset:256 sc1
	v_cndmask_b32_e64 v118, v118, 2, s[74:75]
	v_pk_mul_f32 v[168:169], v[246:247], v[168:169] op_sel_hi:[0,1]
	v_mfma_f32_16x16x4_f32 v[78:81], v255, v25, v[78:81]
	global_load_dwordx4 v[22:25], v104, s[88:89] offset:1024
	v_sub_f32_e32 v121, v178, v114
	v_pk_mul_f32 v[170:171], v[246:247], v[170:171] op_sel_hi:[0,1]
	v_cmp_eq_f32_e64 s[72:73], v178, v114
	global_store_dwordx4 v109, v[168:171], s[90:91] offset:512 sc1
	v_exp_f32_e32 v135, v120
	v_max_f32_dpp v115, v115, v115 row_ror:8 row_mask:0xf bank_mask:0xf
	v_cndmask_b32_e64 v118, v118, 1, s[76:77]
	v_pk_mul_f32 v[172:173], v[246:247], v[172:173] op_sel_hi:[0,1]
	v_exp_f32_e32 v134, v121
	v_pk_mul_f32 v[174:175], v[246:247], v[174:175] op_sel_hi:[0,1]
	v_cndmask_b32_e64 v118, v118, 0, s[72:73]
	global_store_dwordx4 v109, v[172:175], s[90:91] offset:768 sc1
	v_sub_f32_e32 v120, v239, v115
	v_cmp_eq_f32_e64 s[72:73], v239, v115
	s_waitcnt lgkmcnt(0)
	s_waitcnt vmcnt(27)
	v_mfma_f32_16x16x4_f32 v[82:85], v254, v26, 0
	v_sub_f32_e32 v121, v235, v115
	v_add_f32_e32 v250, v240, v250
	v_cmp_eq_f32_e64 s[74:75], v235, v115
	v_add_f32_e32 v251, v241, v251
	v_exp_f32_e32 v175, v120
	v_cndmask_b32_e64 v119, v155, 15, s[72:73]
	v_add_f32_e32 v252, v242, v252
	v_sub_f32_e32 v120, v231, v115
	v_add_f32_e32 v253, v243, v253
	v_cmp_eq_f32_e64 s[76:77], v231, v115
	ds_write2st64_b32 v113, v250, v251 offset1:12
	v_exp_f32_e32 v174, v121
	ds_write2st64_b32 v113, v252, v253 offset0:24 offset1:36
	v_cndmask_b32_e64 v119, v119, 14, s[74:75]
	v_mfma_f32_16x16x4_f32 v[86:89], v254, v28, 0
	v_sub_f32_e32 v121, v227, v115
	v_and_b32_e32 v122, 12, v118
	v_cmp_eq_f32_e64 s[72:73], v227, v115
	v_and_b32_e32 v124, 3, v118
	v_exp_f32_e32 v173, v120
	v_add_f32_e32 v128, v134, v135
	v_cndmask_b32_e64 v119, v119, 13, s[76:77]
	v_sub_f32_e32 v120, v223, v115
	v_add_f32_e32 v130, v136, v137
	v_cmp_eq_f32_e64 s[74:75], v223, v115
	v_lshl_or_b32 v122, v122, 4, v124
	v_exp_f32_e32 v172, v121
	v_add_f32_e32 v128, v128, v138
	v_cndmask_b32_e64 v119, v119, 12, s[72:73]
	v_add_f32_e32 v130, v130, v139
	v_mfma_f32_16x16x4_f32 v[82:85], v255, v27, v[82:85]
	v_sub_f32_e32 v121, v219, v115
	v_cmp_eq_f32_e64 s[76:77], v219, v115
	v_or_b32_e32 v122, v122, v102
	v_exp_f32_e32 v171, v120
	v_add_f32_e32 v128, v128, v140
	v_cndmask_b32_e64 v119, v119, 11, s[74:75]
	v_add_f32_e32 v130, v130, v141
	v_sub_f32_e32 v120, v215, v115
	v_cmp_eq_f32_e64 s[72:73], v215, v115
	v_max_u32_e32 v126, v122, v118
	v_exp_f32_e32 v170, v121
	v_add_f32_e32 v128, v128, v142
	v_cndmask_b32_e64 v119, v119, 10, s[76:77]
	v_add_f32_e32 v130, v130, v143
	v_mfma_f32_16x16x4_f32 v[86:89], v255, v29, v[86:89]
	global_load_dwordx4 v[26:29], v104, s[88:89] offset:2048
	v_sub_f32_e32 v121, v211, v115
	v_min_u32_dpp v126, v126, v126 row_ror:1 row_mask:0xf bank_mask:0xf
	v_cmp_eq_f32_e64 s[74:75], v211, v115
	v_exp_f32_e32 v169, v120
	v_add_f32_e32 v128, v128, v144
	v_cndmask_b32_e64 v119, v119, 9, s[72:73]
	v_add_f32_e32 v130, v130, v145
	v_sub_f32_e32 v120, v207, v115
	v_min_u32_dpp v126, v126, v126 row_ror:2 row_mask:0xf bank_mask:0xf
	v_cmp_eq_f32_e64 s[76:77], v207, v115
	v_add_f32_e32 v128, v128, v146
	v_exp_f32_e32 v168, v121
	v_cndmask_b32_e64 v119, v119, 8, s[74:75]
	v_add_f32_e32 v130, v130, v147
	s_waitcnt vmcnt(24)
	v_mfma_f32_16x16x4_f32 v[90:93], v254, v30, 0
	v_sub_f32_e32 v121, v203, v115
	v_min_u32_dpp v126, v126, v126 row_ror:4 row_mask:0xf bank_mask:0xf
	v_cmp_eq_f32_e64 s[72:73], v203, v115
	v_add_f32_e32 v128, v128, v148
	v_exp_f32_e32 v167, v120
	v_cndmask_b32_e64 v119, v119, 7, s[76:77]
	v_add_f32_e32 v130, v130, v149
	v_sub_f32_e32 v120, v199, v115
	v_min_u32_dpp v126, v126, v126 row_ror:8 row_mask:0xf bank_mask:0xf
	v_cmp_eq_f32_e64 s[74:75], v199, v115
	v_add_f32_e32 v128, v128, v130
	v_exp_f32_e32 v166, v121
	v_mad_u32_u24 v248, v126, 24, v107
	v_cndmask_b32_e64 v119, v119, 6, s[72:73]
	v_mfma_f32_16x16x4_f32 v[94:97], v254, v32, 0
	v_sub_f32_e32 v121, v195, v115
	v_add_f32_dpp v128, v128, v128 row_ror:1 row_mask:0xf bank_mask:0xf
	v_cmp_eq_f32_e64 s[76:77], v195, v115
	global_load_dword v157, v248, s[92:93]
	v_exp_f32_e32 v165, v120
	v_add_f32_dpp v128, v128, v128 row_ror:2 row_mask:0xf bank_mask:0xf
	v_cndmask_b32_e64 v119, v119, 5, s[74:75]
	v_sub_f32_e32 v120, v191, v115
	v_add_f32_dpp v128, v128, v128 row_ror:4 row_mask:0xf bank_mask:0xf
	v_cmp_eq_f32_e64 s[72:73], v191, v115
	s_nop 0
	v_add_f32_dpp v128, v128, v128 row_ror:8 row_mask:0xf bank_mask:0xf
	v_exp_f32_e32 v164, v121
	v_rcp_f32_e32 v244, v128
	v_cndmask_b32_e64 v119, v119, 4, s[76:77]
	v_pk_mul_f32 v[134:135], v[244:245], v[134:135] op_sel_hi:[0,1]
	v_mfma_f32_16x16x4_f32 v[90:93], v255, v31, v[90:93]
	v_sub_f32_e32 v121, v187, v115
	v_cmp_eq_f32_e64 s[74:75], v187, v115
	v_pk_mul_f32 v[136:137], v[244:245], v[136:137] op_sel_hi:[0,1]
	v_exp_f32_e32 v163, v120
	global_store_dwordx4 v110, v[134:137], s[90:91] sc1
	v_cndmask_b32_e64 v119, v119, 3, s[72:73]
	v_pk_mul_f32 v[138:139], v[244:245], v[138:139] op_sel_hi:[0,1]
	v_sub_f32_e32 v120, v183, v115
	v_cmp_eq_f32_e64 s[76:77], v183, v115
	v_pk_mul_f32 v[140:141], v[244:245], v[140:141] op_sel_hi:[0,1]
	v_exp_f32_e32 v162, v121
	global_store_dwordx4 v110, v[138:141], s[90:91] offset:256 sc1
	v_cndmask_b32_e64 v119, v119, 2, s[74:75]
	v_pk_mul_f32 v[142:143], v[244:245], v[142:143] op_sel_hi:[0,1]
	v_mfma_f32_16x16x4_f32 v[94:97], v255, v33, v[94:97]
	global_load_dwordx4 v[30:33], v104, s[88:89] offset:3072
	v_sub_f32_e32 v121, v179, v115
	v_pk_mul_f32 v[144:145], v[244:245], v[144:145] op_sel_hi:[0,1]
	v_cmp_eq_f32_e64 s[72:73], v179, v115
	v_exp_f32_e32 v161, v120
	global_store_dwordx4 v110, v[142:145], s[90:91] offset:512 sc1
	v_cndmask_b32_e64 v119, v119, 1, s[76:77]
	v_pk_mul_f32 v[146:147], v[244:245], v[146:147] op_sel_hi:[0,1]
	v_exp_f32_e32 v160, v121
	v_pk_mul_f32 v[148:149], v[244:245], v[148:149] op_sel_hi:[0,1]
	v_cndmask_b32_e64 v119, v119, 0, s[72:73]
	global_store_dwordx4 v110, v[146:149], s[90:91] offset:768 sc1
	v_and_b32_e32 v123, 12, v119
	v_max3_f32 v114, v34, v38, v42
	v_and_b32_e32 v125, 3, v119
	v_add_f32_e32 v129, v160, v161
	v_add_f32_e32 v131, v162, v163
	v_max3_f32 v116, v46, v50, v54
	v_lshl_or_b32 v123, v123, 4, v125
	v_add_f32_e32 v129, v129, v164
	v_add_f32_e32 v131, v131, v165
	v_or_b32_e32 v123, v123, v102
	v_max3_f32 v114, v114, v58, v62
	v_add_f32_e32 v129, v129, v166
	v_add_f32_e32 v131, v131, v167
	v_max_u32_e32 v127, v123, v119
	v_max3_f32 v116, v116, v66, v70
	v_add_f32_e32 v129, v129, v168
	v_add_f32_e32 v131, v131, v169
	v_min_u32_dpp v127, v127, v127 row_ror:1 row_mask:0xf bank_mask:0xf
	v_add_f32_e32 v129, v129, v170
	v_max3_f32 v114, v114, v74, v78
	v_add_f32_e32 v131, v131, v171
	v_min_u32_dpp v127, v127, v127 row_ror:2 row_mask:0xf bank_mask:0xf
	v_add_f32_e32 v129, v129, v172
	v_max3_f32 v116, v116, v82, v86
	v_add_f32_e32 v131, v131, v173
	v_min_u32_dpp v127, v127, v127 row_ror:4 row_mask:0xf bank_mask:0xf
	v_add_f32_e32 v129, v129, v174
	v_add_f32_e32 v131, v131, v175
	v_max3_f32 v114, v114, v90, v94
	v_min_u32_dpp v127, v127, v127 row_ror:8 row_mask:0xf bank_mask:0xf
	v_add_f32_e32 v129, v129, v131
	v_mad_u32_u24 v249, v127, 24, v107
	s_nop 0
	v_add_f32_dpp v129, v129, v129 row_ror:1 row_mask:0xf bank_mask:0xf
	v_max_f32_e32 v114, v114, v116
	global_load_dword v156, v249, s[92:93]
	v_add_f32_dpp v129, v129, v129 row_ror:2 row_mask:0xf bank_mask:0xf
	s_nop 1
	v_add_f32_dpp v129, v129, v129 row_ror:4 row_mask:0xf bank_mask:0xf
	v_max_f32_dpp v114, v114, v114 row_ror:1 row_mask:0xf bank_mask:0xf
	s_nop 0
	v_add_f32_dpp v129, v129, v129 row_ror:8 row_mask:0xf bank_mask:0xf
	v_rcp_f32_e32 v246, v129
	s_nop 0
	v_pk_mul_f32 v[160:161], v[246:247], v[160:161] op_sel_hi:[0,1]
	v_pk_mul_f32 v[162:163], v[246:247], v[162:163] op_sel_hi:[0,1]
	v_max_f32_dpp v114, v114, v114 row_ror:2 row_mask:0xf bank_mask:0xf
	global_store_dwordx4 v111, v[160:163], s[90:91] sc1
	v_pk_mul_f32 v[164:165], v[246:247], v[164:165] op_sel_hi:[0,1]
	v_pk_mul_f32 v[166:167], v[246:247], v[166:167] op_sel_hi:[0,1]
	v_max_f32_dpp v114, v114, v114 row_ror:4 row_mask:0xf bank_mask:0xf
	global_store_dwordx4 v111, v[164:167], s[90:91] offset:256 sc1
	v_pk_mul_f32 v[168:169], v[246:247], v[168:169] op_sel_hi:[0,1]
	v_pk_mul_f32 v[170:171], v[246:247], v[170:171] op_sel_hi:[0,1]
	global_store_dwordx4 v111, v[168:171], s[90:91] offset:512 sc1
	v_max_f32_dpp v114, v114, v114 row_ror:8 row_mask:0xf bank_mask:0xf
	v_pk_mul_f32 v[172:173], v[246:247], v[172:173] op_sel_hi:[0,1]
	v_pk_mul_f32 v[174:175], v[246:247], v[174:175] op_sel_hi:[0,1]
	global_store_dwordx4 v111, v[172:175], s[90:91] offset:768 sc1
	s_add_i32 s70, s70, 1
	s_cmp_lt_u32 s70, 16
	s_cbranch_scc1 .Lk3m_loop
